# attn conv blocks: LN gain/shift loads issued before tile loads; column-sum loop split over 4 waves
# baseline (speedup 1.0000x reference)
.LBB2_33:
	s_waitcnt lgkmcnt(0)
	s_ashr_i32 s0, s19, 6
	s_abs_i32 s1, s0
	v_cvt_f32_u32_e32 v1, s1
	s_sub_i32 s17, 0, s1
	s_sub_i32 s2, s2, s3
	s_abs_i32 s16, s2
	v_rcp_iflag_f32_e32 v1, v1
	s_xor_b32 s3, s2, s0
	s_ashr_i32 s3, s3, 31
	s_waitcnt vmcnt(9)
	v_and_b32_e32 v2, 63, v0
	v_mul_f32_e32 v1, 0x4f7ffffe, v1
	v_cvt_u32_f32_e32 v1, v1
	v_lshlrev_b32_e32 v2, 2, v2
	v_mov_b32_e32 v3, 0
	v_cmp_gt_u32_e32 vcc, 64, v0
	v_readfirstlane_b32 s18, v1
	s_mul_i32 s17, s17, s18
	s_mul_hi_u32 s17, s18, s17
	s_add_i32 s18, s18, s17
	s_mul_hi_u32 s17, s16, s18
	s_mul_i32 s18, s17, s1
	s_sub_i32 s16, s16, s18
	s_add_i32 s23, s17, 1
	s_sub_i32 s18, s16, s1
	s_cmp_ge_u32 s16, s1
	s_cselect_b32 s17, s23, s17
	s_cselect_b32 s16, s18, s16
	s_add_i32 s18, s17, 1
	s_cmp_ge_u32 s16, s1
	s_cselect_b32 s1, s18, s17
	s_xor_b32 s1, s1, s3
	s_sub_i32 s1, s1, s3
	s_mul_i32 s0, s1, s0
	s_sub_i32 s0, s2, s0
	s_lshl_b32 s16, s0, 6
	s_ashr_i32 s17, s16, 31
	s_lshl_b32 s18, s1, 6
	s_lshl_b64 s[2:3], s[16:17], 2
	v_lshrrev_b32_e32 v1, 6, v0
	s_add_u32 s0, s20, s2
	s_addc_u32 s1, s21, s3
	s_waitcnt vmcnt(3)
	v_or_b32_e32 v22, s18, v1
	v_add_u32_e32 v23, s18, v1
	v_lshl_add_u64 v[4:5], s[0:1], 0, v[2:3]
	v_mad_i64_i32 v[6:7], s[0:1], v22, s19, 0
	v_add_u32_e32 v8, 4, v23
	v_add_u32_e32 v10, 8, v23
	v_add_u32_e32 v12, 12, v23
	v_or_b32_e32 v14, 16, v22
	v_add_u32_e32 v16, 20, v23
	v_add_u32_e32 v18, 24, v23
	v_add_u32_e32 v20, 28, v23
	v_lshl_add_u64 v[6:7], v[6:7], 2, v[4:5]
	v_mad_i64_i32 v[8:9], s[0:1], v8, s19, 0
	v_mad_i64_i32 v[10:11], s[0:1], v10, s19, 0
	v_mad_i64_i32 v[12:13], s[0:1], v12, s19, 0
	v_mad_i64_i32 v[14:15], s[0:1], v14, s19, 0
	v_mad_i64_i32 v[16:17], s[0:1], v16, s19, 0
	v_mad_i64_i32 v[18:19], s[0:1], v18, s19, 0
	v_mad_i64_i32 v[20:21], s[0:1], v20, s19, 0
	v_lshl_add_u64 v[8:9], v[8:9], 2, v[4:5]
	v_lshl_add_u64 v[10:11], v[10:11], 2, v[4:5]
	v_lshl_add_u64 v[12:13], v[12:13], 2, v[4:5]
	v_lshl_add_u64 v[14:15], v[14:15], 2, v[4:5]
	v_lshl_add_u64 v[16:17], v[16:17], 2, v[4:5]
	v_lshl_add_u64 v[18:19], v[18:19], 2, v[4:5]
	v_lshl_add_u64 v[20:21], v[20:21], 2, v[4:5]
	s_cmp_lg_u64 s[14:15], 0
	s_cbranch_scc0 .Lcv_nog
	v_and_b32_e32 v56, 63, v0
	v_or_b32_e32 v56, s18, v56
	v_mov_b32_e32 v57, 0
	v_lshlrev_b64 v[56:57], 2, v[56:57]
	v_lshl_add_u64 v[58:59], s[4:5], 0, v[56:57]
	v_lshl_add_u64 v[56:57], s[6:7], 0, v[56:57]
	global_load_dword v60, v[58:59], off
	global_load_dword v61, v[56:57], off
.Lcv_nog:
	global_load_dword v24, v[6:7], off nt
	global_load_dword v25, v[8:9], off nt
	global_load_dword v26, v[10:11], off nt
	global_load_dword v27, v[12:13], off nt
	global_load_dword v28, v[14:15], off nt
	global_load_dword v29, v[16:17], off nt
	global_load_dword v30, v[18:19], off nt
	global_load_dword v31, v[20:21], off nt
	v_or_b32_e32 v6, 32, v22
	v_mad_i64_i32 v[6:7], s[0:1], v6, s19, 0
	v_add_u32_e32 v8, 36, v23
	v_add_u32_e32 v10, 40, v23
	v_add_u32_e32 v12, 44, v23
	v_or_b32_e32 v14, 48, v22
	v_add_u32_e32 v16, 52, v23
	v_add_u32_e32 v18, 56, v23
	v_add_u32_e32 v20, 60, v23
	v_lshl_add_u64 v[6:7], v[6:7], 2, v[4:5]
	v_mad_i64_i32 v[8:9], s[0:1], v8, s19, 0
	v_mad_i64_i32 v[10:11], s[0:1], v10, s19, 0
	v_mad_i64_i32 v[12:13], s[0:1], v12, s19, 0
	v_mad_i64_i32 v[14:15], s[0:1], v14, s19, 0
	v_mad_i64_i32 v[16:17], s[0:1], v16, s19, 0
	v_mad_i64_i32 v[18:19], s[0:1], v18, s19, 0
	v_mad_i64_i32 v[20:21], s[0:1], v20, s19, 0
	v_lshl_add_u64 v[8:9], v[8:9], 2, v[4:5]
	v_lshl_add_u64 v[10:11], v[10:11], 2, v[4:5]
	v_lshl_add_u64 v[12:13], v[12:13], 2, v[4:5]
	v_lshl_add_u64 v[14:15], v[14:15], 2, v[4:5]
	v_lshl_add_u64 v[16:17], v[16:17], 2, v[4:5]
	v_lshl_add_u64 v[18:19], v[18:19], 2, v[4:5]
	v_lshl_add_u64 v[4:5], v[20:21], 2, v[4:5]
	global_load_dword v20, v[6:7], off nt
	global_load_dword v21, v[8:9], off nt
	global_load_dword v22, v[10:11], off nt
	global_load_dword v23, v[12:13], off nt
	global_load_dword v32, v[14:15], off nt
	global_load_dword v33, v[16:17], off nt
	global_load_dword v34, v[18:19], off nt
	global_load_dword v35, v[4:5], off nt
	s_movk_i32 s0, 0x104
	s_cmp_lg_u64 s[8:9], 0
	v_mul_lo_u32 v1, v1, s0
	s_cselect_b64 s[0:1], -1, 0
	s_and_b64 s[20:21], s[14:15], s[0:1]
	v_add3_u32 v1, 0, v2, v1
	s_and_b64 s[14:15], s[20:21], vcc
	s_waitcnt vmcnt(15)
	ds_write_b32 v1, v24
	s_waitcnt vmcnt(14)
	ds_write_b32 v1, v25 offset:1040
	s_waitcnt vmcnt(13)
	ds_write_b32 v1, v26 offset:2080
	s_waitcnt vmcnt(12)
	ds_write_b32 v1, v27 offset:3120
	s_waitcnt vmcnt(11)
	ds_write_b32 v1, v28 offset:4160
	s_waitcnt vmcnt(10)
	ds_write_b32 v1, v29 offset:5200
	s_waitcnt vmcnt(9)
	ds_write_b32 v1, v30 offset:6240
	s_waitcnt vmcnt(8)
	ds_write_b32 v1, v31 offset:7280
	s_waitcnt vmcnt(7)
	ds_write_b32 v1, v20 offset:8320
	s_waitcnt vmcnt(6)
	ds_write_b32 v1, v21 offset:9360
	s_waitcnt vmcnt(5)
	ds_write_b32 v1, v22 offset:10400
	s_waitcnt vmcnt(4)
	ds_write_b32 v1, v23 offset:11440
	s_waitcnt vmcnt(3)
	ds_write_b32 v1, v32 offset:12480
	s_waitcnt vmcnt(2)
	ds_write_b32 v1, v33 offset:13520
	s_waitcnt vmcnt(1)
	ds_write_b32 v1, v34 offset:14560
	s_waitcnt vmcnt(0)
	ds_write_b32 v1, v35 offset:15600
	s_and_saveexec_b64 s[0:1], s[14:15]
	s_cbranch_execz .LBB2_35
	v_lshl_add_u32 v2, v0, 2, 0
	ds_write2st64_b32 v2, v60, v61 offset0:65 offset1:66

.LBB2_39:
	v_lshrrev_b32_e32 v3, 5, v0
	v_mul_u32_u24_e32 v2, 0x208, v1
	v_lshlrev_b32_e32 v6, 2, v1
	v_lshlrev_b32_e32 v1, 2, v3
	v_add3_u32 v1, 0, v2, v1
	ds_read2_b32 v[8:9], v1 offset1:8
	ds_read2_b32 v[10:11], v1 offset0:65 offset1:73
	s_ashr_i32 s19, s18, 31
	s_lshl_b64 s[0:1], s[18:19], 1
	s_add_u32 s0, s12, s0
	v_mov_b32_e32 v2, 0
	s_waitcnt lgkmcnt(1)
	v_mov_b32_e32 v12, v8
	s_waitcnt lgkmcnt(0)
	v_mov_b32_e32 v13, v10
	s_addc_u32 s1, s13, s1
	v_mov_b32_e32 v7, v2
	v_pk_mul_f32 v[12:13], v[4:5], v[12:13]
	v_or_b32_e32 v14, s16, v3
	v_lshl_add_u64 v[6:7], s[0:1], 0, v[6:7]
	v_cvt_pk_f16_f32 v8, v12, v13
	v_mad_i64_i32 v[12:13], s[0:1], v14, s22, 0
	v_lshl_add_u64 v[12:13], v[12:13], 1, v[6:7]
	v_mov_b32_e32 v10, v9
	global_store_dword v[12:13], v8, off
	v_pk_mul_f32 v[8:9], v[4:5], v[10:11]
	v_add_u32_e32 v3, s16, v3
	v_cvt_pk_f16_f32 v15, v8, v9
	ds_read2_b32 v[8:9], v1 offset0:16 offset1:24
	ds_read2_b32 v[10:11], v1 offset0:81 offset1:89
	v_add_u32_e32 v12, 8, v3
	v_mad_i64_i32 v[12:13], s[0:1], v12, s22, 0
	v_lshl_add_u64 v[12:13], v[12:13], 1, v[6:7]
	global_store_dword v[12:13], v15, off
	s_waitcnt lgkmcnt(1)
	v_mov_b32_e32 v12, v8
	s_waitcnt lgkmcnt(0)
	v_mov_b32_e32 v13, v10
	v_pk_mul_f32 v[12:13], v[4:5], v[12:13]
	v_add_u32_e32 v10, 16, v3
	v_cvt_pk_f16_f32 v8, v12, v13
	v_mad_i64_i32 v[12:13], s[0:1], v10, s22, 0
	v_lshl_add_u64 v[12:13], v[12:13], 1, v[6:7]
	v_mov_b32_e32 v10, v9
	global_store_dword v[12:13], v8, off
	v_pk_mul_f32 v[8:9], v[4:5], v[10:11]
	v_add_u32_e32 v12, 24, v3
	v_cvt_pk_f16_f32 v15, v8, v9
	ds_read2_b32 v[8:9], v1 offset0:32 offset1:40
	ds_read2_b32 v[10:11], v1 offset0:97 offset1:105
	v_mad_i64_i32 v[12:13], s[0:1], v12, s22, 0
	v_lshl_add_u64 v[12:13], v[12:13], 1, v[6:7]
	global_store_dword v[12:13], v15, off
	s_waitcnt lgkmcnt(1)
	v_mov_b32_e32 v12, v8
	s_waitcnt lgkmcnt(0)
	v_mov_b32_e32 v13, v10
	v_pk_mul_f32 v[12:13], v[4:5], v[12:13]
	v_or_b32_e32 v10, 32, v14
	v_cvt_pk_f16_f32 v8, v12, v13
	v_mad_i64_i32 v[12:13], s[0:1], v10, s22, 0
	v_lshl_add_u64 v[12:13], v[12:13], 1, v[6:7]
	v_mov_b32_e32 v10, v9
	global_store_dword v[12:13], v8, off
	v_pk_mul_f32 v[8:9], v[4:5], v[10:11]
	v_add_u32_e32 v12, 40, v3
	v_cvt_pk_f16_f32 v14, v8, v9
	ds_read2_b32 v[8:9], v1 offset0:48 offset1:56
	ds_read2_b32 v[10:11], v1 offset0:113 offset1:121
	v_mad_i64_i32 v[12:13], s[0:1], v12, s22, 0
	v_lshl_add_u64 v[12:13], v[12:13], 1, v[6:7]
	global_store_dword v[12:13], v14, off
	s_waitcnt lgkmcnt(1)
	v_mov_b32_e32 v12, v8
	s_waitcnt lgkmcnt(0)
	v_mov_b32_e32 v13, v10
	v_pk_mul_f32 v[12:13], v[4:5], v[12:13]
	v_add_u32_e32 v8, 48, v3
	v_cvt_pk_f16_f32 v1, v12, v13
	v_mad_i64_i32 v[12:13], s[0:1], v8, s22, 0
	v_mov_b32_e32 v10, v9
	v_lshl_add_u64 v[12:13], v[12:13], 1, v[6:7]
	v_pk_mul_f32 v[4:5], v[4:5], v[10:11]
	v_add_u32_e32 v3, 56, v3
	global_store_dword v[12:13], v1, off
	v_cvt_pk_f16_f32 v1, v4, v5
	v_mad_i64_i32 v[4:5], s[0:1], v3, s22, 0
	v_lshl_add_u64 v[4:5], v[4:5], 1, v[6:7]
	global_store_dword v[4:5], v1, off
	s_and_saveexec_b64 s[0:1], s[20:21]
	s_cbranch_execz .LBB2_43
	v_lshrrev_b32_e32 v4, 6, v0
	v_and_b32_e32 v0, 63, v0
	v_readfirstlane_b32 s1, v4
	v_lshlrev_b32_e32 v1, 2, v0
	s_nop 1
	s_mul_i32 s0, s1, 0x1040
	v_add_u32_e32 v1, s0, v1
	s_lshl_b32 s1, s1, 6
	s_add_i32 s0, s1, 0x4100
	v_mov_b32_e32 v3, v2
.LBB2_41:
	v_add_u32_e32 v4, 0, v1
	ds_read2_b32 v[36:37], v4 offset1:65
	s_add_i32 s1, s0, 0
	ds_read2_b32 v[38:39], v4 offset0:130 offset1:195
	v_mov_b32_e32 v32, s1
	v_add_u32_e32 v28, 0x400, v4
	v_add_u32_e32 v29, 0x800, v4
	v_add_u32_e32 v50, 0xc00, v4
	ds_read_b128 v[4:7], v32
	ds_read_b128 v[8:11], v32 offset:16
	ds_read_b128 v[12:15], v32 offset:32
	ds_read_b128 v[16:19], v32 offset:48
	ds_read2_b32 v[40:41], v28 offset0:4 offset1:69
	ds_read_b128 v[20:23], v32 offset:256
	ds_read_b128 v[24:27], v32 offset:272
	ds_read2_b32 v[42:43], v28 offset0:134 offset1:199
	ds_read2_b32 v[44:45], v29 offset0:8 offset1:73
	ds_read2_b32 v[46:47], v29 offset0:138 offset1:203
	ds_read2_b32 v[48:49], v50 offset0:12 offset1:77
	ds_read_b128 v[28:31], v32 offset:288
	ds_read_b128 v[32:35], v32 offset:304
	ds_read2_b32 v[50:51], v50 offset0:142 offset1:207
	s_waitcnt lgkmcnt(13)
	v_fma_mixlo_f16 v4, v36, v4, 0
	s_waitcnt lgkmcnt(8)
	v_mul_f32_e32 v53, v36, v20
	v_fma_mixlo_f16 v20, v37, v5, 0
	v_cvt_f32_f16_e32 v52, v4
	v_fma_mixlo_f16 v6, v38, v6, 0
	v_cvt_f32_f16_e32 v4, v20
	v_mul_f32_e32 v5, v37, v21
	v_mul_f32_e32 v21, v38, v22
	v_fma_mixlo_f16 v22, v39, v7, 0
	v_cvt_f32_f16_e32 v20, v6
	v_fma_mixlo_f16 v8, v40, v8, 0
	v_cvt_f32_f16_e32 v6, v22
	v_mul_f32_e32 v7, v39, v23
	s_waitcnt lgkmcnt(7)
	v_mul_f32_e32 v23, v40, v24
	v_fma_mixlo_f16 v24, v41, v9, 0
	v_cvt_f32_f16_e32 v22, v8
	v_pk_add_f32 v[2:3], v[2:3], v[52:53]
	s_waitcnt lgkmcnt(6)
	v_fma_mixlo_f16 v10, v42, v10, 0
	v_cvt_f32_f16_e32 v8, v24
	v_pk_add_f32 v[2:3], v[2:3], v[4:5]
	v_mul_f32_e32 v9, v41, v25
	v_mul_f32_e32 v25, v42, v26
	v_fma_mixlo_f16 v26, v43, v11, 0
	v_cvt_f32_f16_e32 v24, v10
	v_pk_add_f32 v[2:3], v[2:3], v[20:21]
	s_waitcnt lgkmcnt(5)
	v_fma_mixlo_f16 v12, v44, v12, 0
	v_cvt_f32_f16_e32 v10, v26
	v_pk_add_f32 v[2:3], v[2:3], v[6:7]
	v_mul_f32_e32 v11, v43, v27
	s_waitcnt lgkmcnt(2)
	v_mul_f32_e32 v27, v44, v28
	v_fma_mixlo_f16 v28, v45, v13, 0
	v_cvt_f32_f16_e32 v26, v12
	v_pk_add_f32 v[2:3], v[2:3], v[22:23]
	v_fma_mixlo_f16 v14, v46, v14, 0
	v_cvt_f32_f16_e32 v12, v28
	v_pk_add_f32 v[2:3], v[2:3], v[8:9]
	v_mul_f32_e32 v13, v45, v29
	v_mul_f32_e32 v29, v46, v30
	v_fma_mixlo_f16 v30, v47, v15, 0
	v_cvt_f32_f16_e32 v28, v14
	v_pk_add_f32 v[2:3], v[2:3], v[24:25]
	v_fma_mixlo_f16 v16, v48, v16, 0
	v_cvt_f32_f16_e32 v14, v30
	v_pk_add_f32 v[2:3], v[2:3], v[10:11]
	v_mul_f32_e32 v15, v47, v31
	s_waitcnt lgkmcnt(1)
	v_mul_f32_e32 v31, v48, v32
	v_fma_mixlo_f16 v32, v49, v17, 0
	v_cvt_f32_f16_e32 v30, v16
	v_pk_add_f32 v[2:3], v[2:3], v[26:27]
	s_waitcnt lgkmcnt(0)
	v_fma_mixlo_f16 v18, v50, v18, 0
	v_cvt_f32_f16_e32 v16, v32
	v_pk_add_f32 v[2:3], v[2:3], v[12:13]
	v_mul_f32_e32 v17, v49, v33
	v_mul_f32_e32 v33, v50, v34
	v_fma_mixlo_f16 v34, v51, v19, 0
	v_cvt_f32_f16_e32 v32, v18
	v_pk_add_f32 v[2:3], v[2:3], v[28:29]
	v_cvt_f32_f16_e32 v18, v34
	v_pk_add_f32 v[2:3], v[2:3], v[14:15]
	s_add_i32 s0, s0, 64
	v_pk_add_f32 v[2:3], v[2:3], v[30:31]
	v_mul_f32_e32 v19, v51, v35
	v_pk_add_f32 v[2:3], v[2:3], v[16:17]
	v_add_u32_e32 v1, 0x1040, v1
	v_pk_add_f32 v[2:3], v[2:3], v[32:33]
	s_cmpk_eq_i32 s0, 0x4200
	v_pk_add_f32 v[2:3], v[2:3], v[18:19]
	s_add_u32 s0, s8, s2
	v_mov_b32_e32 v1, 0
	s_addc_u32 s1, s9, s3
	v_lshlrev_b64 v[0:1], 2, v[0:1]
	v_lshl_add_u64 v[4:5], s[0:1], 0, v[0:1]
	s_add_u32 s0, s10, s2
	s_addc_u32 s1, s11, s3
	global_atomic_add_f32 v[4:5], v2, off
	v_lshl_add_u64 v[0:1], s[0:1], 0, v[0:1]
	global_atomic_add_f32 v[0:1], v3, off
